# baseline (speedup 1.0000x reference)
_Z8pam_mainPKDv4_jS1_S1_PKfS3_PDF16_Pf:
	s_load_dwordx8 s[4:11], s[0:1], 0x0
	s_load_dwordx4 s[12:15], s[0:1], 0x20
	s_load_dwordx2 s[16:17], s[0:1], 0x30
	v_and_b32_e32 v1, 63, v0
	v_lshrrev_b32_e32 v3, 6, v0
	v_lshlrev_b32_e32 v2, 4, v1
	v_lshlrev_b32_e32 v4, 2, v1
	v_readfirstlane_b32 s18, v3
	v_and_b32_e32 v3, 31, v1
	v_lshlrev_b32_e32 v5, 2, v3
	s_mul_i32 s19, s2, 54
	s_mul_i32 s20, s2, 3
	s_lshr_b32 s20, s20, 4
	s_mul_i32 s21, s20, 0x120
	s_sub_u32 s21, s19, s21
	s_cmp_ge_u32 s20, 24
	s_cselect_b32 s22, 0x120, 0
	s_add_u32 s22, s22, s21
	s_add_u32 s23, s20, 1
	s_cmp_ge_u32 s23, 24
	s_cselect_b32 s24, 0x120, 0
	s_sub_u32 s25, 0x120, s21
	s_cmp_lt_u32 s25, 54
	s_cselect_b32 s26, 1, 0
	s_mul_i32 s25, s25, 43
	s_lshr_b32 s25, s25, 8
	s_cmp_eq_u32 s26, 1
	s_cselect_b32 s25, s25, 100
	s_mov_b32 s29, s2
	s_mov_b32 s46, 0
	s_mov_b32 s47, 30720
	s_mov_b32 s48, 61440
	s_mov_b32 s27, 0
	s_mov_b32 s28, 1
	s_mul_i32 s30, s18, 0xd00
	s_add_u32 s30, s30, 92160
	v_add_u32_e32 v7, s30, v2
	v_mul_u32_u24_e32 v6, 0x68, v3
	v_lshrrev_b32_e32 v130, 2, v1
	v_and_b32_e32 v130, 8, v130
	v_add3_u32 v6, v6, v130, s30
	v_mov_b32_e32 v150, 0xf149f2ca
	s_waitcnt lgkmcnt(0)
	global_load_dwordx4 v[132:135], v2, s[12:13]
	global_load_dwordx4 v[136:139], v2, s[12:13] offset:1024
	global_load_dword v140, v4, s[12:13] offset:2048
	s_mul_i32 s30, s20, 12
	s_add_u32 s30, s30, s18
	s_add_u32 s31, s20, s26
	s_mul_i32 s31, s31, 12
	s_add_u32 s31, s31, s18
	s_lshl_b32 s36, s30, 10
	s_add_u32 s56, s6, s36
	s_addc_u32 s57, s7, 0
	s_lshl_b32 s36, s31, 10
	s_add_u32 s58, s6, s36
	s_addc_u32 s59, s7, 0
	global_load_dwordx4 v[8:11], v2, s[56:57]
	global_load_dwordx4 v[12:15], v2, s[58:59]
	s_lshl_b32 s36, s30, 7
	s_add_u32 s60, s10, s36
	s_addc_u32 s61, s11, 0
	s_lshl_b32 s36, s31, 7
	s_add_u32 s62, s10, s36
	s_addc_u32 s63, s11, 0
	global_load_dword v141, v5, s[60:61]
	global_load_dword v142, v5, s[62:63]
	s_lshl_b32 s33, s18, 10
	s_lshl_b32 s30, s22, 12
	s_add_u32 s30, s30, s33
	s_add_u32 s50, s8, s30
	s_addc_u32 s51, s9, 0
	s_lshl_b32 s30, s22, 10
	s_add_u32 s30, s30, s33
	s_add_u32 s54, s4, s30
	s_addc_u32 s55, s5, 0
	s_lshl_b32 s30, s24, 12
	s_add_u32 s30, s30, s33
	s_add_u32 s64, s8, s30
	s_addc_u32 s65, s9, 0
	s_lshl_b32 s30, s24, 10
	s_add_u32 s30, s30, s33
	s_add_u32 s66, s4, s30
	s_addc_u32 s67, s5, 0
	s_cmp_eq_u32 s27, s25
	s_cbranch_scc0 .Lm_ns_p0
	s_mov_b64 s[50:51], s[64:65]
	s_mov_b64 s[54:55], s[66:67]

.Lm_nok_p0:
	s_add_u32 s50, s50, 0x6000
	s_addc_u32 s51, s51, 0
	s_add_u32 s54, s54, 0x1800
	s_addc_u32 s55, s55, 0
	s_cmp_eq_u32 s28, s25
	s_cbranch_scc0 .Lm_ns_p1
	s_mov_b64 s[50:51], s[64:65]
	s_mov_b64 s[54:55], s[66:67]

.Lm_nok_p1:
	s_add_u32 s50, s50, 0x6000
	s_addc_u32 s51, s51, 0
	s_add_u32 s54, s54, 0x1800
	s_addc_u32 s55, s55, 0
	s_waitcnt vmcnt(4)
	s_nop 0
	v_max3_f32 v132, v132, v133, v134
	v_max3_f32 v136, v136, v137, v138
	v_max3_f32 v132, v132, v135, v139
	v_max3_f32 v132, v132, v136, v140
	s_nop 1
	v_max_f32_dpp v132, v132, v132 quad_perm:[1,0,3,2] row_mask:0xf bank_mask:0xf
	s_nop 1
	v_max_f32_dpp v132, v132, v132 quad_perm:[2,3,0,1] row_mask:0xf bank_mask:0xf
	s_nop 1
	v_max_f32_dpp v132, v132, v132 row_half_mirror row_mask:0xf bank_mask:0xf
	s_nop 1
	v_max_f32_dpp v132, v132, v132 row_mirror row_mask:0xf bank_mask:0xf
	s_nop 1
	v_readlane_b32 s36, v132, 0
	v_readlane_b32 s37, v132, 16
	v_readlane_b32 s38, v132, 32
	v_readlane_b32 s39, v132, 48
	s_nop 2
	v_mov_b32_e32 v133, s36
	v_max_f32_e32 v133, s37, v133
	v_max_f32_e32 v133, s38, v133
	v_max_f32_e32 v133, s39, v133
	s_mov_b32 s37, 0xf800000
	v_mul_f32_e32 v137, 0x4f800000, v133
	v_cmp_gt_f32_e32 vcc, s37, v133
	s_nop 1
	v_cndmask_b32_e32 v133, v133, v137, vcc
	v_sqrt_f32_e32 v137, v133
	s_nop 0
	v_add_u32_e32 v138, -1, v137
	v_add_u32_e32 v139, 1, v137
	v_fma_f32 v143, -v138, v137, v133
	v_fma_f32 v144, -v139, v137, v133
	v_cmp_ge_f32_e64 s[38:39], 0, v143
	s_nop 1
	v_cndmask_b32_e64 v137, v137, v138, s[38:39]
	v_cmp_lt_f32_e64 s[38:39], 0, v144
	s_nop 1
	v_cndmask_b32_e64 v137, v137, v139, s[38:39]
	v_mul_f32_e32 v138, 0x37800000, v137
	v_cndmask_b32_e32 v137, v137, v138, vcc
	v_mov_b32_e32 v138, 0x260
	v_cmp_class_f32_e32 vcc, v133, v138
	s_nop 1
	v_cndmask_b32_e32 v133, v137, v133, vcc
	v_mov_b32_e32 v135, 0x3ca3d70a
	s_mov_b32 s36, 0xffff
	v_mul_f32_e32 v134, v141, v133
	v_mul_f32_e32 v136, v142, v133
	v_fmamk_f32 v134, v134, 0x3f804189, v135
	v_fmamk_f32 v136, v136, 0x3f804189, v135
	v_cvt_f16_f32_e64 v134, -v134
	v_cvt_f16_f32_e64 v136, -v136
	v_cmp_gt_u32_e32 vcc, 32, v1
	v_cvt_f32_f16_e32 v148, v134
	v_cvt_f32_f16_e32 v149, v136
	v_bfi_b32 v134, s36, v134, v11
	v_bfi_b32 v136, s36, v136, v15
	v_cndmask_b32_e32 v11, v11, v134, vcc
	v_cndmask_b32_e32 v15, v15, v136, vcc
	s_waitcnt vmcnt(0)
	s_barrier
	s_mov_b32 s28, 2
	v_add_u32_e32 v128, s46, v2
	v_add_u32_e32 v129, s47, v2
	ds_read_b128 v[88:91], v128 offset:24576
	ds_read_b128 v[92:95], v128 offset:25600
	ds_read_b128 v[96:99], v128 offset:0
	ds_read_b128 v[104:107], v128 offset:2048
	ds_read_b128 v[100:103], v128 offset:1024
	ds_read_b128 v[108:111], v128 offset:3072
	s_cmp_eq_u32 s28, s25
	s_cbranch_scc0 .Lm_ns_p2
	s_mov_b64 s[50:51], s[64:65]
	s_mov_b64 s[54:55], s[66:67]
